# attention: one static s_setprio 1 for waves 4-7 across P4 (reset at the phase exit)
# baseline (speedup 1.0000x reference)
; template <bool MLA>
; __device__ __forceinline__ void attn_unit(char* lds, int h, int qb, const bf16_t* Qp, int ldq, const bf16_t* Kp, int ldk, const bf16_t* KRp, const bf16_t* Vp, int ldv,
;                                           unsigned char* Op, int ldo, const float* KMp, const float* rel_bias) {
;     ...
;     const int tid = threadIdx.x, wid = __builtin_amdgcn_readfirstlane(tid >> 6), lane = tid & 63, r32 = lane & 31, hi = lane >> 5;
;     float* wsf = (float*)(lds + OFF_WS) + wid * 64; float* li_l = wsf; float* al_l = wsf + 32; const float* al_h = al_l + 4 * hi; const float* li_h = li_l + 4 * hi;
;     unsigned* sel_l = (unsigned*)(lds + OFF_SEL); float* bt_l = (float*)(lds + OFF_BT); float* km_l = (float*)(lds + OFF_KM);
;     const int q0 = qb * 256, qlo = q0 + wid * 32, qpos = qlo + r32, NT = (qb + 1) * 4;
;     unsigned offKn[2], offV[2], offKr;
; #pragma unroll
;     for (int i = 0; i < 2; ++i) { const int pc = wid * 2 + i;
;         { const int row = pc * 4 + (lane >> 4), colB = ((lane & 15) * 16) ^ ((row & 7) << 4); offKn[i] = (unsigned)(row * ldk + (colB >> 1)); }
;         { const int sub = pc * 2 + (lane >> 5), kk = (sub >> 2) * 8 + ((lane & 31) >> 2), c = (sub & 3) * 32 + (lane & 3) * 8; const int k = (kk & ~0xC) | ((kk & 4) << 1) | ((kk & 8) >> 1);
;           offV[i] = (unsigned)(k * ldv + c); } }
;     { const int row = wid * 8 + (lane >> 3), colB = ((lane & 7) * 16) ^ ((row & 7) << 4); offKr = (unsigned)(row * 64 + (colB >> 1)); }
; __global__ void __launch_bounds__(512, 2) mega_fwd(Args args) {
;     ...
;     if (IN(4)) {
;     ...
;         for (;;) { if (tid == 0) MISC[12] = atomicAdd(ctl + CW_AQ1, 1u);
;             __syncthreads(); const int it = (int)MISC[12]; __syncthreads();
;             if (it >= 512) break;
;             const int qb = 15 - (it >> 5), bh = it & 31, b = bh >> 3, hh = bh & 7;
.LBB0_1373:
	s_add_u32 s70, s18, 0x4a000000
	s_addc_u32 s71, s19, 0
	s_cmp_lt_i32 s20, 5
	s_cselect_b64 s[4:5], -1, 0
	s_cmp_gt_i32 s21, 4
	s_cselect_b64 s[6:7], -1, 0
	s_and_b64 s[36:37], s[4:5], s[6:7]
	s_andn2_b64 vcc, exec, s[36:37]
	s_cbranch_vccnz .LBB0_1778
	v_lshrrev_b32_e32 v186, 4, v164
	s_waitcnt vmcnt(15)
	v_and_b32_e32 v2, 15, v0
	v_bitop3_b32 v2, v186, v2, 4 bitop3:0x36
	v_bitop3_b32 v4, v186, v0, 15 bitop3:0x78
	v_lshlrev_b32_e32 v193, 3, v2
	v_lshrrev_b32_e32 v2, 3, v164
	v_lshlrev_b32_e32 v191, 3, v4
	v_bitop3_b32 v4, v2, v0, 7 bitop3:0x78
	v_lshrrev_b32_e32 v3, 5, v164
	v_lshlrev_b32_e32 v4, 3, v4
	v_lshl_or_b32 v158, v2, 6, v4
	v_lshlrev_b32_e32 v4, 4, v3
	s_waitcnt lgkmcnt(0)
	v_lshlrev_b32_e32 v5, 4, v0
	s_movk_i32 s3, 0x70
	s_add_u32 s8, s18, 0xc300
	s_waitcnt vmcnt(14)
	v_and_b32_e32 v6, 0x70, v5
	v_bitop3_b32 v154, v4, v5, s3 bitop3:0x78
	s_movk_i32 s3, 0x60
	s_addc_u32 s9, s19, 0
	v_bitop3_b32 v155, v4, v6, 32 bitop3:0x36
	v_bitop3_b32 v156, v4, v6, 64 bitop3:0x36
	v_bitop3_b32 v157, v4, v6, s3 bitop3:0x36
	v_and_b32_e32 v4, 0xc0, v5
	v_lshlrev_b32_e32 v5, 1, v0
	v_and_b32_e32 v168, 31, v0
	v_lshlrev_b32_e32 v165, 2, v3
	v_lshlrev_b32_e32 v152, 3, v0
	v_and_b32_e32 v5, 32, v5
	s_movk_i32 s3, 0x118
	s_cmp_lg_u32 0, -1
	v_lshlrev_b32_e32 v2, 3, v3
	v_and_or_b32 v5, v152, s3, v5
	s_cselect_b32 s3, 0, 0
	v_lshlrev_b32_e32 v170, 13, v3
	v_sub_u32_e32 v3, v168, v165
	v_and_b32_e32 v150, 32, v0
	v_and_b32_e32 v151, 24, v152
	v_lshrrev_b32_e32 v189, 1, v0
	v_mov_b32_e32 v147, 0
	v_mov_b32_e32 v7, 0x10000
	v_add3_u32 v194, v4, s3, v5
	v_and_b32_e32 v4, 3, v0
	v_add_u32_e32 v160, 0xee5, v3
	s_add_i32 s3, 0, 0x25170
	v_mbcnt_lo_u32_b32 v3, -1, 0
	v_bfe_u32 v187, v0, 2, 3
	v_or_b32_e32 v188, v150, v151
	v_and_b32_e32 v190, 8, v189
	v_or_b32_e32 v192, 4, v186
	v_lshlrev_b32_e32 v153, 8, v168
	v_lshl_or_b32 v159, v168, 7, v7
	v_cmp_gt_u32_e64 s[4:5], 32, v164
	s_mov_b32 s11, 0
	v_cmp_eq_u32_e64 s[6:7], 0, v4
	v_mov_b32_e32 v169, v147
	v_mov_b32_e32 v171, v147
	v_mov_b32_e32 v161, s3
	s_movk_i32 s16, 0x1ff
	s_movk_i32 s17, 0xc00
	s_mov_b64 s[38:39], 0x100
	s_mov_b64 s[40:41], 0x180
	s_mov_b32 s26, 0x41000000
	v_mbcnt_hi_u32_b32 v195, -1, v3
	v_mov_b32_e32 v162, 0x1ffff3
	v_lshlrev_b32_e32 v172, 1, v2
	v_mov_b32_e32 v163, 0xff800000
	s_mov_b64 s[98:99], exec
	s_and_b64 exec, exec, s[14:15]
	v_mov_b32_e32 v254, 0
	v_mov_b32_e32 v253, 1
	s_nop 0
	global_atomic_add v253, v254, v253, s[8:9] sc0
	s_mov_b64 exec, s[98:99]
	v_readfirstlane_b32 s98, v0
	s_nop 3
	s_and_b32 s98, s98, 0x3ff
	s_lshr_b32 s98, s98, 6
	s_cmp_ge_u32 s98, 4
	s_cbranch_scc0 .Lattn_prio_done
	s_setprio 1
.Lattn_prio_done:
	s_branch .LBB0_1377
.LBB0_1375:
	s_or_b64 exec, exec, s[42:43]
	s_mov_b64 s[42:43], 0
	s_waitcnt lgkmcnt(0)
	s_barrier

; __global__ void __launch_bounds__(512, 2) mega_fwd(Args args) {
;     ...
;         if (ovl && tid == 0) __hip_atomic_store(ctl + CW_STOP, 1u, RLX_AGENT);
.LBB0_1775:
	s_setprio 0
	s_and_b64 s[6:7], s[14:15], s[34:35]
	s_and_saveexec_b64 s[4:5], s[6:7]
	s_cbranch_execz .LBB0_1777
	v_mov_b32_e32 v1, 0xc000
	v_mov_b32_e32 v2, 1
	global_store_dword v1, v2, s[18:19] offset:256 sc1
